# stack3 + GLA state scan (G2): each 8-step block issues its 16 loads up front with counted waits, stores batched at the block end (was: every step waits for its own loads)
# speedup vs baseline: 1.0094x; 1.0041x over previous
; __device__ __forceinline__ unsigned pk2(float lo, float hi) { return f2bf(lo) | (f2bf(hi) << 16); }
; __device__ __forceinline__ float bflo(unsigned w) { return __uint_as_float(w << 16); }
; __device__ __forceinline__ float bfhi(unsigned w) { return __uint_as_float(w & 0xffff0000u); }
; __device__ __forceinline__ void gla_g2(bf16* ST, const float* DEC, int gid) {
;     ...
;     bf16* p = ST + (((size_t)bh * 64) * 256 + c) * 128 + k4; const float* dp = DEC + (size_t)bh * 64 * 128 + k4;
; #pragma unroll 8
;     for (int n = 0; n < 64; ++n) {
;         const v2u d = *(const v2u*)(p + (size_t)n * 256 * 128); const f32x4 dc = *(const f32x4*)(dp + n * 128);
;         v2u w; w.x = pk2(s0, s1); w.y = pk2(s2, s3); *(v2u*)(p + (size_t)n * 256 * 128) = w;
;         s0 = dc.x * s0 + bflo(d.x); s1 = dc.y * s1 + bfhi(d.x); s2 = dc.z * s2 + bflo(d.y); s3 = dc.w * s3 + bfhi(d.y); }
.LBB0_1039:
	v_lshl_add_u64 v[160:161], v[2:3], 0, s[14:15]
	global_load_dwordx2 v[100:101], v[160:161], off
	global_load_dwordx4 v[120:123], v[4:5], off offset:-3584
	s_mov_b64 s[98:99], 0x10000
	v_lshl_add_u64 v[162:163], v[160:161], 0, s[98:99]
	global_load_dwordx2 v[102:103], v[162:163], off
	global_load_dwordx4 v[124:127], v[4:5], off offset:-3072
	s_mov_b64 s[98:99], 0x20000
	v_lshl_add_u64 v[164:165], v[160:161], 0, s[98:99]
	global_load_dwordx2 v[104:105], v[164:165], off
	global_load_dwordx4 v[128:131], v[4:5], off offset:-2560
	s_mov_b64 s[98:99], 0x30000
	v_lshl_add_u64 v[166:167], v[160:161], 0, s[98:99]
	global_load_dwordx2 v[106:107], v[166:167], off
	global_load_dwordx4 v[132:135], v[4:5], off offset:-2048
	s_mov_b64 s[98:99], 0x40000
	v_lshl_add_u64 v[168:169], v[160:161], 0, s[98:99]
	global_load_dwordx2 v[108:109], v[168:169], off
	global_load_dwordx4 v[136:139], v[4:5], off offset:-1536
	s_mov_b64 s[98:99], 0x50000
	v_lshl_add_u64 v[170:171], v[160:161], 0, s[98:99]
	global_load_dwordx2 v[110:111], v[170:171], off
	global_load_dwordx4 v[140:143], v[4:5], off offset:-1024
	s_mov_b64 s[98:99], 0x60000
	v_lshl_add_u64 v[172:173], v[160:161], 0, s[98:99]
	global_load_dwordx2 v[112:113], v[172:173], off
	global_load_dwordx4 v[144:147], v[4:5], off offset:-512
	s_mov_b64 s[98:99], 0x70000
	v_lshl_add_u64 v[174:175], v[160:161], 0, s[98:99]
	global_load_dwordx2 v[114:115], v[174:175], off
	global_load_dwordx4 v[148:151], v[4:5], off
	v_and_b32_sdwa v77, v11, v224 dst_sel:DWORD dst_unused:UNUSED_PAD src0_sel:WORD_1 src1_sel:DWORD
	v_and_b32_sdwa v76, v9, v224 dst_sel:DWORD dst_unused:UNUSED_PAD src0_sel:WORD_1 src1_sel:DWORD
	v_and_b32_sdwa v79, v10, v224 dst_sel:DWORD dst_unused:UNUSED_PAD src0_sel:WORD_1 src1_sel:DWORD
	v_and_b32_sdwa v78, v8, v224 dst_sel:DWORD dst_unused:UNUSED_PAD src0_sel:WORD_1 src1_sel:DWORD
	v_add3_u32 v77, v11, v77, s40
	v_add3_u32 v76, v9, v76, s40
	v_add3_u32 v78, v8, v78, s40
	v_add3_u32 v79, v10, v79, s40
	v_and_b32_e32 v77, 0xffff0000, v77
	v_and_b32_e32 v76, 0xffff0000, v76
	v_or_b32_sdwa v181, v77, v79 dst_sel:DWORD dst_unused:UNUSED_PAD src0_sel:DWORD src1_sel:WORD_1
	v_or_b32_sdwa v180, v76, v78 dst_sel:DWORD dst_unused:UNUSED_PAD src0_sel:DWORD src1_sel:WORD_1
	s_waitcnt vmcnt(14)
	v_lshlrev_b32_e32 v80, 16, v100
	v_and_b32_e32 v81, 0xffff0000, v100
	v_pk_fma_f32 v[8:9], v[8:9], v[120:121], v[80:81]
	v_lshlrev_b32_e32 v82, 16, v101
	v_and_b32_e32 v83, 0xffff0000, v101
	v_pk_fma_f32 v[10:11], v[10:11], v[122:123], v[82:83]
	v_and_b32_sdwa v77, v11, v224 dst_sel:DWORD dst_unused:UNUSED_PAD src0_sel:WORD_1 src1_sel:DWORD
	v_and_b32_sdwa v76, v9, v224 dst_sel:DWORD dst_unused:UNUSED_PAD src0_sel:WORD_1 src1_sel:DWORD
	v_and_b32_sdwa v79, v10, v224 dst_sel:DWORD dst_unused:UNUSED_PAD src0_sel:WORD_1 src1_sel:DWORD
	v_and_b32_sdwa v78, v8, v224 dst_sel:DWORD dst_unused:UNUSED_PAD src0_sel:WORD_1 src1_sel:DWORD
	v_add3_u32 v77, v11, v77, s40
	v_add3_u32 v76, v9, v76, s40
	v_add3_u32 v78, v8, v78, s40
	v_add3_u32 v79, v10, v79, s40
	v_and_b32_e32 v77, 0xffff0000, v77
	v_and_b32_e32 v76, 0xffff0000, v76
	v_or_b32_sdwa v183, v77, v79 dst_sel:DWORD dst_unused:UNUSED_PAD src0_sel:DWORD src1_sel:WORD_1
	v_or_b32_sdwa v182, v76, v78 dst_sel:DWORD dst_unused:UNUSED_PAD src0_sel:DWORD src1_sel:WORD_1
	s_waitcnt vmcnt(12)
	v_lshlrev_b32_e32 v80, 16, v102
	v_and_b32_e32 v81, 0xffff0000, v102
	v_pk_fma_f32 v[8:9], v[8:9], v[124:125], v[80:81]
	v_lshlrev_b32_e32 v82, 16, v103
	v_and_b32_e32 v83, 0xffff0000, v103
	v_pk_fma_f32 v[10:11], v[10:11], v[126:127], v[82:83]
	v_and_b32_sdwa v77, v11, v224 dst_sel:DWORD dst_unused:UNUSED_PAD src0_sel:WORD_1 src1_sel:DWORD
	v_and_b32_sdwa v76, v9, v224 dst_sel:DWORD dst_unused:UNUSED_PAD src0_sel:WORD_1 src1_sel:DWORD
	v_and_b32_sdwa v79, v10, v224 dst_sel:DWORD dst_unused:UNUSED_PAD src0_sel:WORD_1 src1_sel:DWORD
	v_and_b32_sdwa v78, v8, v224 dst_sel:DWORD dst_unused:UNUSED_PAD src0_sel:WORD_1 src1_sel:DWORD
	v_add3_u32 v77, v11, v77, s40
	v_add3_u32 v76, v9, v76, s40
	v_add3_u32 v78, v8, v78, s40
	v_add3_u32 v79, v10, v79, s40
	v_and_b32_e32 v77, 0xffff0000, v77
	v_and_b32_e32 v76, 0xffff0000, v76
	v_or_b32_sdwa v185, v77, v79 dst_sel:DWORD dst_unused:UNUSED_PAD src0_sel:DWORD src1_sel:WORD_1
	v_or_b32_sdwa v184, v76, v78 dst_sel:DWORD dst_unused:UNUSED_PAD src0_sel:DWORD src1_sel:WORD_1
	s_waitcnt vmcnt(10)
	v_lshlrev_b32_e32 v80, 16, v104
	v_and_b32_e32 v81, 0xffff0000, v104
	v_pk_fma_f32 v[8:9], v[8:9], v[128:129], v[80:81]
	v_lshlrev_b32_e32 v82, 16, v105
	v_and_b32_e32 v83, 0xffff0000, v105
	v_pk_fma_f32 v[10:11], v[10:11], v[130:131], v[82:83]
	v_and_b32_sdwa v77, v11, v224 dst_sel:DWORD dst_unused:UNUSED_PAD src0_sel:WORD_1 src1_sel:DWORD
	v_and_b32_sdwa v76, v9, v224 dst_sel:DWORD dst_unused:UNUSED_PAD src0_sel:WORD_1 src1_sel:DWORD
	v_and_b32_sdwa v79, v10, v224 dst_sel:DWORD dst_unused:UNUSED_PAD src0_sel:WORD_1 src1_sel:DWORD
	v_and_b32_sdwa v78, v8, v224 dst_sel:DWORD dst_unused:UNUSED_PAD src0_sel:WORD_1 src1_sel:DWORD
	v_add3_u32 v77, v11, v77, s40
	v_add3_u32 v76, v9, v76, s40
	v_add3_u32 v78, v8, v78, s40
	v_add3_u32 v79, v10, v79, s40
	v_and_b32_e32 v77, 0xffff0000, v77
	v_and_b32_e32 v76, 0xffff0000, v76
	v_or_b32_sdwa v187, v77, v79 dst_sel:DWORD dst_unused:UNUSED_PAD src0_sel:DWORD src1_sel:WORD_1
	v_or_b32_sdwa v186, v76, v78 dst_sel:DWORD dst_unused:UNUSED_PAD src0_sel:DWORD src1_sel:WORD_1
	s_waitcnt vmcnt(8)
; __device__ __forceinline__ unsigned pk2(float lo, float hi) { return f2bf(lo) | (f2bf(hi) << 16); }
; __device__ __forceinline__ float bflo(unsigned w) { return __uint_as_float(w << 16); }
; __device__ __forceinline__ float bfhi(unsigned w) { return __uint_as_float(w & 0xffff0000u); }
; __device__ __forceinline__ void gla_g2(bf16* ST, const float* DEC, int gid) {
;     ...
;     bf16* p = ST + (((size_t)bh * 64) * 256 + c) * 128 + k4; const float* dp = DEC + (size_t)bh * 64 * 128 + k4;
; #pragma unroll 8
;     for (int n = 0; n < 64; ++n) {
;         const v2u d = *(const v2u*)(p + (size_t)n * 256 * 128); const f32x4 dc = *(const f32x4*)(dp + n * 128);
;         v2u w; w.x = pk2(s0, s1); w.y = pk2(s2, s3); *(v2u*)(p + (size_t)n * 256 * 128) = w;
;         s0 = dc.x * s0 + bflo(d.x); s1 = dc.y * s1 + bfhi(d.x); s2 = dc.z * s2 + bflo(d.y); s3 = dc.w * s3 + bfhi(d.y); }
	v_lshlrev_b32_e32 v80, 16, v106
	v_and_b32_e32 v81, 0xffff0000, v106
	v_pk_fma_f32 v[8:9], v[8:9], v[132:133], v[80:81]
	v_lshlrev_b32_e32 v82, 16, v107
	v_and_b32_e32 v83, 0xffff0000, v107
	v_pk_fma_f32 v[10:11], v[10:11], v[134:135], v[82:83]
	v_and_b32_sdwa v77, v11, v224 dst_sel:DWORD dst_unused:UNUSED_PAD src0_sel:WORD_1 src1_sel:DWORD
	v_and_b32_sdwa v76, v9, v224 dst_sel:DWORD dst_unused:UNUSED_PAD src0_sel:WORD_1 src1_sel:DWORD
	v_and_b32_sdwa v79, v10, v224 dst_sel:DWORD dst_unused:UNUSED_PAD src0_sel:WORD_1 src1_sel:DWORD
	v_and_b32_sdwa v78, v8, v224 dst_sel:DWORD dst_unused:UNUSED_PAD src0_sel:WORD_1 src1_sel:DWORD
	v_add3_u32 v77, v11, v77, s40
	v_add3_u32 v76, v9, v76, s40
	v_add3_u32 v78, v8, v78, s40
	v_add3_u32 v79, v10, v79, s40
	v_and_b32_e32 v77, 0xffff0000, v77
	v_and_b32_e32 v76, 0xffff0000, v76
	v_or_b32_sdwa v189, v77, v79 dst_sel:DWORD dst_unused:UNUSED_PAD src0_sel:DWORD src1_sel:WORD_1
	v_or_b32_sdwa v188, v76, v78 dst_sel:DWORD dst_unused:UNUSED_PAD src0_sel:DWORD src1_sel:WORD_1
	s_waitcnt vmcnt(6)
	v_lshlrev_b32_e32 v80, 16, v108
	v_and_b32_e32 v81, 0xffff0000, v108
	v_pk_fma_f32 v[8:9], v[8:9], v[136:137], v[80:81]
	v_lshlrev_b32_e32 v82, 16, v109
	v_and_b32_e32 v83, 0xffff0000, v109
	v_pk_fma_f32 v[10:11], v[10:11], v[138:139], v[82:83]
	v_and_b32_sdwa v77, v11, v224 dst_sel:DWORD dst_unused:UNUSED_PAD src0_sel:WORD_1 src1_sel:DWORD
	v_and_b32_sdwa v76, v9, v224 dst_sel:DWORD dst_unused:UNUSED_PAD src0_sel:WORD_1 src1_sel:DWORD
	v_and_b32_sdwa v79, v10, v224 dst_sel:DWORD dst_unused:UNUSED_PAD src0_sel:WORD_1 src1_sel:DWORD
	v_and_b32_sdwa v78, v8, v224 dst_sel:DWORD dst_unused:UNUSED_PAD src0_sel:WORD_1 src1_sel:DWORD
	v_add3_u32 v77, v11, v77, s40
	v_add3_u32 v76, v9, v76, s40
	v_add3_u32 v78, v8, v78, s40
	v_add3_u32 v79, v10, v79, s40
	v_and_b32_e32 v77, 0xffff0000, v77
	v_and_b32_e32 v76, 0xffff0000, v76
	v_or_b32_sdwa v191, v77, v79 dst_sel:DWORD dst_unused:UNUSED_PAD src0_sel:DWORD src1_sel:WORD_1
	v_or_b32_sdwa v190, v76, v78 dst_sel:DWORD dst_unused:UNUSED_PAD src0_sel:DWORD src1_sel:WORD_1
	s_waitcnt vmcnt(4)
	v_lshlrev_b32_e32 v80, 16, v110
	v_and_b32_e32 v81, 0xffff0000, v110
	v_pk_fma_f32 v[8:9], v[8:9], v[140:141], v[80:81]
	v_lshlrev_b32_e32 v82, 16, v111
	v_and_b32_e32 v83, 0xffff0000, v111
	v_pk_fma_f32 v[10:11], v[10:11], v[142:143], v[82:83]
	v_and_b32_sdwa v77, v11, v224 dst_sel:DWORD dst_unused:UNUSED_PAD src0_sel:WORD_1 src1_sel:DWORD
	v_and_b32_sdwa v76, v9, v224 dst_sel:DWORD dst_unused:UNUSED_PAD src0_sel:WORD_1 src1_sel:DWORD
	v_and_b32_sdwa v79, v10, v224 dst_sel:DWORD dst_unused:UNUSED_PAD src0_sel:WORD_1 src1_sel:DWORD
	v_and_b32_sdwa v78, v8, v224 dst_sel:DWORD dst_unused:UNUSED_PAD src0_sel:WORD_1 src1_sel:DWORD
	v_add3_u32 v77, v11, v77, s40
	v_add3_u32 v76, v9, v76, s40
	v_add3_u32 v78, v8, v78, s40
	v_add3_u32 v79, v10, v79, s40
	v_and_b32_e32 v77, 0xffff0000, v77
	v_and_b32_e32 v76, 0xffff0000, v76
	v_or_b32_sdwa v193, v77, v79 dst_sel:DWORD dst_unused:UNUSED_PAD src0_sel:DWORD src1_sel:WORD_1
	v_or_b32_sdwa v192, v76, v78 dst_sel:DWORD dst_unused:UNUSED_PAD src0_sel:DWORD src1_sel:WORD_1
	s_waitcnt vmcnt(2)
	v_lshlrev_b32_e32 v80, 16, v112
	v_and_b32_e32 v81, 0xffff0000, v112
	v_pk_fma_f32 v[8:9], v[8:9], v[144:145], v[80:81]
	v_lshlrev_b32_e32 v82, 16, v113
	v_and_b32_e32 v83, 0xffff0000, v113
	v_pk_fma_f32 v[10:11], v[10:11], v[146:147], v[82:83]
	v_and_b32_sdwa v77, v11, v224 dst_sel:DWORD dst_unused:UNUSED_PAD src0_sel:WORD_1 src1_sel:DWORD
	v_and_b32_sdwa v76, v9, v224 dst_sel:DWORD dst_unused:UNUSED_PAD src0_sel:WORD_1 src1_sel:DWORD
	v_and_b32_sdwa v79, v10, v224 dst_sel:DWORD dst_unused:UNUSED_PAD src0_sel:WORD_1 src1_sel:DWORD
	v_and_b32_sdwa v78, v8, v224 dst_sel:DWORD dst_unused:UNUSED_PAD src0_sel:WORD_1 src1_sel:DWORD
	v_add3_u32 v77, v11, v77, s40
	v_add3_u32 v76, v9, v76, s40
	v_add3_u32 v78, v8, v78, s40
	v_add3_u32 v79, v10, v79, s40
	v_and_b32_e32 v77, 0xffff0000, v77
	v_and_b32_e32 v76, 0xffff0000, v76
	v_or_b32_sdwa v195, v77, v79 dst_sel:DWORD dst_unused:UNUSED_PAD src0_sel:DWORD src1_sel:WORD_1
	v_or_b32_sdwa v194, v76, v78 dst_sel:DWORD dst_unused:UNUSED_PAD src0_sel:DWORD src1_sel:WORD_1
	s_waitcnt vmcnt(0)
	v_lshlrev_b32_e32 v80, 16, v114
	v_and_b32_e32 v81, 0xffff0000, v114
	v_pk_fma_f32 v[8:9], v[8:9], v[148:149], v[80:81]
	v_lshlrev_b32_e32 v82, 16, v115
	v_and_b32_e32 v83, 0xffff0000, v115
	v_pk_fma_f32 v[10:11], v[10:11], v[150:151], v[82:83]
	global_store_dwordx2 v[160:161], v[180:181], off
	global_store_dwordx2 v[162:163], v[182:183], off
	global_store_dwordx2 v[164:165], v[184:185], off
	global_store_dwordx2 v[166:167], v[186:187], off
	global_store_dwordx2 v[168:169], v[188:189], off
	global_store_dwordx2 v[170:171], v[190:191], off
	global_store_dwordx2 v[172:173], v[192:193], off
	global_store_dwordx2 v[174:175], v[194:195], off
	s_mov_b64 s[98:99], 0x1000
	v_lshl_add_u64 v[4:5], v[4:5], 0, s[98:99]
	s_add_u32 s14, s14, 0x80000
	s_addc_u32 s15, s15, 0
	s_cmp_lg_u32 s14, 0x400000
	s_cbranch_scc1 .LBB0_1039
	v_add_u32_e32 v0, s82, v0
	s_mov_b32 s0, 0x1ffff
	v_cmp_lt_i32_e32 vcc, s0, v0
	v_readlane_b32 s0, v254, 22
	s_or_b64 s[12:13], vcc, s[12:13]
	s_nop 0
	v_add_u32_e32 v14, s0, v14
	s_andn2_b64 exec, exec, s[12:13]
	s_cbranch_execnz .LBB0_1038
